# SSD output gate: the two loop-invariant norm-weight loads that sat behind each row's stores (a drain plus a round trip each) are issued at the top of the row
# baseline (speedup 1.0000x reference)
.LBB0_1174:
	global_load_dwordx4 v[142:145], v[8:9], off offset:1024
	global_load_dwordx4 v[146:149], v[8:9], off offset:2048
	v_lshl_add_u64 v[20:21], s[16:17], 0, v[6:7]
	v_add_co_u32_e32 v38, vcc, 0x53c00000, v20
	v_lshl_add_u64 v[24:25], s[14:15], 0, v[6:7]
	s_nop 0
	v_addc_co_u32_e32 v39, vcc, 0, v21, vcc
	v_add_co_u32_e32 v20, vcc, 0x57200000, v20
	v_lshl_add_u64 v[26:27], s[12:13], 0, v[6:7]
	s_nop 0
	v_addc_co_u32_e32 v21, vcc, 0, v21, vcc
	v_add_co_u32_e32 v24, vcc, 0x9d00000, v24
	global_load_dword v16, v[10:11], off
	global_load_dword v18, v[12:13], off
	global_load_dword v22, v[14:15], off
	global_load_dwordx4 v[2:5], v[8:9], off
	v_addc_co_u32_e32 v25, vcc, 0, v25, vcc
	global_load_dwordx2 v[40:41], v[38:39], off
	global_load_dwordx2 v[42:43], v[38:39], off offset:512
	global_load_dwordx2 v[44:45], v[20:21], off
	global_load_dwordx2 v[46:47], v[20:21], off offset:512
	global_load_dwordx2 v[48:49], v[20:21], off offset:1024
	global_load_dwordx2 v[50:51], v[38:39], off offset:1024
	v_add_co_u32_e32 v20, vcc, 0x34400000, v26
	global_load_dwordx2 v[38:39], v[24:25], off
	global_load_dwordx2 v[52:53], v[24:25], off offset:512
	global_load_dwordx2 v[54:55], v[24:25], off offset:1024
	v_addc_co_u32_e32 v21, vcc, 0, v27, vcc
	global_load_dwordx2 v[24:25], v[20:21], off
	global_load_dwordx2 v[26:27], v[20:21], off offset:512
	global_load_dwordx2 v[56:57], v[20:21], off offset:1024
	v_lshl_add_u64 v[28:29], s[8:9], 0, v[6:7]
	v_add_co_u32_e64 v28, s[6:7], s23, v28
	s_add_i32 s2, s2, s4
	s_nop 0
	v_addc_co_u32_e64 v29, s[6:7], 0, v29, s[6:7]
	s_add_u32 s8, s8, s10
	s_addc_u32 s9, s9, s11
	s_add_u32 s12, s12, s3
	s_addc_u32 s13, s13, s5
	s_add_u32 s14, s14, s18
	s_addc_u32 s15, s15, s19
	s_add_u32 s16, s16, s20
	s_addc_u32 s17, s17, s21
	s_cmp_lt_i32 s2, 0x9000
	s_waitcnt vmcnt(9)
	v_lshlrev_b32_e32 v23, 16, v44
	v_lshlrev_b32_e32 v17, 16, v40
	v_and_b32_e32 v58, 0xffff0000, v41
	v_lshlrev_b32_e32 v19, 16, v42
	v_and_b32_e32 v59, 0xffff0000, v45
	s_waitcnt vmcnt(8)
	v_lshlrev_b32_e32 v37, 16, v46
	s_waitcnt vmcnt(5)
	v_lshlrev_b32_e32 v72, 16, v39
	v_and_b32_e32 v74, 0xffff0000, v39
	s_waitcnt vmcnt(2)
	v_lshlrev_b32_e32 v71, 16, v24
	v_and_b32_e32 v39, 0xffff0000, v24
	s_waitcnt vmcnt(1)
	v_lshlrev_b32_e32 v77, 16, v26
	v_lshlrev_b32_e32 v60, 16, v43
	v_and_b32_e32 v62, 0xffff0000, v43
	v_and_b32_e32 v43, 0xffff0000, v46
	v_add_f32_e32 v46, v23, v17
	v_pk_add_f32 v[58:59], v[58:59], v[58:59] op_sel:[1,0] op_sel_hi:[0,1]
	v_add_f32_e32 v68, v37, v19
	v_lshlrev_b32_e32 v73, 16, v25
	v_lshlrev_b32_e32 v79, 16, v27
	v_and_b32_e32 v81, 0xffff0000, v27
	s_waitcnt vmcnt(0)
	v_lshlrev_b32_e32 v83, 16, v56
	v_mul_f32_e32 v17, 0xbfb8aa3b, v71
	v_mul_f32_e32 v19, 0xbfb8aa3b, v39
	v_mul_f32_e32 v27, 0xbfb8aa3b, v77
	v_lshlrev_b32_e32 v61, 16, v47
	v_and_b32_e32 v63, 0xffff0000, v47
	v_lshlrev_b32_e32 v47, 16, v50
	v_and_b32_e32 v59, 0xffff0000, v50
	v_mul_f32_e32 v23, 0xbfb8aa3b, v73
	v_mul_f32_e32 v50, 0xbfb8aa3b, v83
	v_exp_f32_e32 v17, v17
	v_exp_f32_e32 v19, v19
	v_exp_f32_e32 v27, v27
	v_exp_f32_e32 v23, v23
	v_exp_f32_e32 v50, v50
	v_and_b32_e32 v20, 0xffff0000, v40
	v_lshlrev_b32_e32 v40, 16, v41
	v_lshlrev_b32_e32 v41, 16, v45
	v_lshlrev_b32_e32 v78, 16, v53
	v_and_b32_e32 v80, 0xffff0000, v53
	v_and_b32_e32 v53, 0xffff0000, v26
	v_and_b32_e32 v21, 0xffff0000, v44
	v_lshlrev_b32_e32 v45, 16, v48
	v_and_b32_e32 v65, 0xffff0000, v48
	v_lshlrev_b32_e32 v67, 16, v49
	v_and_b32_e32 v49, 0xffff0000, v49
	v_mov_b32_e32 v44, v41
	v_mov_b32_e32 v48, v61
	v_pk_add_f32 v[62:63], v[62:63], v[62:63] op_sel:[1,0] op_sel_hi:[0,1]
	v_lshlrev_b32_e32 v84, 16, v55
	v_and_b32_e32 v86, 0xffff0000, v55
	v_and_b32_e32 v75, 0xffff0000, v25
	v_and_b32_e32 v55, 0xffff0000, v56
	v_mul_f32_e32 v37, 0xbfb8aa3b, v53
	v_and_b32_e32 v69, 0xffff0000, v51
	v_pk_add_f32 v[40:41], v[44:45], v[40:41]
	v_pk_add_f32 v[24:25], v[48:49], v[60:61]
	v_lshlrev_b32_e32 v63, 16, v51
	v_lshlrev_b32_e32 v85, 16, v57
	v_and_b32_e32 v87, 0xffff0000, v57
	v_mul_f32_e32 v26, 0xbfb8aa3b, v75
	v_mul_f32_e32 v44, 0xbfb8aa3b, v79
	v_mul_f32_e32 v51, 0xbfb8aa3b, v55
	v_exp_f32_e32 v37, v37
	v_add_f32_e32 v17, 1.0, v17
	v_add_f32_e32 v60, 1.0, v19
	v_add_f32_e32 v19, 1.0, v27
	v_mul_f32_e32 v56, 0xbfb8aa3b, v85
	v_mul_f32_e32 v57, 0xbfb8aa3b, v87
	v_exp_f32_e32 v26, v26
	v_exp_f32_e32 v44, v44
	v_exp_f32_e32 v51, v51
	v_add_f32_e32 v64, 1.0, v23
	v_add_f32_e32 v23, 1.0, v50
	v_rcp_f32_e32 v17, v17
	v_rcp_f32_e32 v19, v19
	v_exp_f32_e32 v56, v56
	v_exp_f32_e32 v57, v57
	v_rcp_f32_e32 v23, v23
	v_mul_f32_e32 v48, 0xbfb8aa3b, v81
	v_lshlrev_b32_e32 v70, 16, v38
	v_lshlrev_b32_e32 v76, 16, v52
	v_exp_f32_e32 v48, v48
	v_add_f32_e32 v37, 1.0, v37
	v_lshlrev_b32_e32 v82, 16, v54
	v_add_f32_e32 v66, 1.0, v26
	v_add_f32_e32 v88, 1.0, v44
	v_add_f32_e32 v44, 1.0, v51
	v_pk_mul_f32 v[26:27], v[16:17], v[70:71]
	v_rcp_f32_e32 v17, v60
	v_pk_mul_f32 v[50:51], v[18:19], v[76:77]
	v_rcp_f32_e32 v19, v37
	v_add_f32_e32 v90, 1.0, v56
	v_add_f32_e32 v91, 1.0, v57
	v_pk_mul_f32 v[56:57], v[22:23], v[82:83]
	v_rcp_f32_e32 v23, v44
	v_and_b32_e32 v42, 0xffff0000, v42
	v_mov_b32_e32 v44, v26
	v_pk_add_f32 v[20:21], v[20:21], v[20:21] op_sel:[1,0] op_sel_hi:[0,1]
	v_and_b32_e32 v38, 0xffff0000, v38
	v_pk_add_f32 v[42:43], v[42:43], v[42:43] op_sel:[1,0] op_sel_hi:[0,1]
	v_and_b32_e32 v52, 0xffff0000, v52
	v_add_f32_e32 v89, 1.0, v48
	v_mov_b32_e32 v48, v50
	v_pk_mov_b32 v[26:27], v[26:27], v[56:57] op_sel:[1,0]
	v_pk_add_f32 v[44:45], v[46:47], v[44:45]
	v_and_b32_e32 v54, 0xffff0000, v54
	v_pk_add_f32 v[46:47], v[68:69], v[48:49]
	v_pk_mul_f32 v[48:49], v[44:45], v[26:27]
	v_pk_add_f32 v[26:27], v[44:45], v[26:27]
	v_pk_fma_f32 v[20:21], v[16:17], v[38:39], v[20:21]
	v_mul_f32_e32 v38, v17, v39
	v_rcp_f32_e32 v17, v64
	v_pk_fma_f32 v[42:43], v[18:19], v[52:53], v[42:43]
	v_mul_f32_e32 v44, v19, v53
	v_rcp_f32_e32 v19, v88
	v_pk_mul_f32 v[52:53], v[22:23], v[54:55]
	v_rcp_f32_e32 v23, v90
	v_mov_b32_e32 v61, v57
	v_mov_b32_e32 v49, v27
	v_mov_b32_e32 v60, v48
	v_pk_mul_f32 v[20:21], v[20:21], v[38:39] op_sel_hi:[1,0]
	v_mov_b32_e32 v71, v57
	v_pk_mul_f32 v[54:55], v[26:27], v[56:57]
	v_pk_mul_f32 v[38:39], v[42:43], v[44:45] op_sel_hi:[1,0]
	v_pk_mul_f32 v[42:43], v[48:49], v[60:61]
	v_mov_b32_e32 v21, v27
	v_mov_b32_e32 v70, v20
	v_pk_mul_f32 v[54:55], v[42:43], v[54:55]
	v_pk_fma_f32 v[60:61], v[20:21], v[70:71], v[42:43]
	v_pk_fma_f32 v[40:41], v[16:17], v[72:73], v[40:41]
	v_mul_f32_e32 v42, v17, v73
	v_rcp_f32_e32 v17, v66
	v_pk_fma_f32 v[24:25], v[18:19], v[78:79], v[24:25]
	v_mul_f32_e32 v44, v19, v79
	v_rcp_f32_e32 v19, v89
	v_pk_mul_f32 v[68:69], v[22:23], v[84:85]
	v_rcp_f32_e32 v23, v91
	v_pk_mul_f32 v[16:17], v[16:17], v[74:75]
	v_pk_mul_f32 v[18:19], v[18:19], v[80:81]
	v_mov_b32_e32 v64, v16
	v_pk_mul_f32 v[22:23], v[22:23], v[86:87]
	v_mov_b32_e32 v66, v18
	v_pk_mov_b32 v[16:17], v[16:17], v[52:53] op_sel:[1,0]
	v_pk_mov_b32 v[18:19], v[18:19], v[68:69] op_sel:[1,0]
	v_pk_mov_b32 v[50:51], v[50:51], v[22:23] op_sel:[1,0]
	v_pk_add_f32 v[58:59], v[58:59], v[64:65]
	v_pk_add_f32 v[62:63], v[62:63], v[66:67]
	v_mov_b32_e32 v45, v53
	v_pk_mul_f32 v[64:65], v[46:47], v[50:51]
	v_pk_add_f32 v[46:47], v[46:47], v[50:51]
	v_pk_mul_f32 v[50:51], v[58:59], v[16:17]
	v_pk_add_f32 v[16:17], v[58:59], v[16:17]
	v_pk_mul_f32 v[58:59], v[62:63], v[18:19]
	v_pk_add_f32 v[18:19], v[62:63], v[18:19]
	v_mov_b32_e32 v61, v55
	v_pk_mul_f32 v[40:41], v[40:41], v[42:43] op_sel_hi:[1,0]
	v_pk_mul_f32 v[24:25], v[24:25], v[44:45] op_sel_hi:[1,0]
	v_mov_b32_e32 v55, v69
	v_mov_b32_e32 v73, v23
	v_mov_b32_e32 v65, v47
	v_mov_b32_e32 v72, v64
	v_mov_b32_e32 v51, v17
	v_mov_b32_e32 v44, v50
	v_mov_b32_e32 v59, v19
	v_mov_b32_e32 v54, v58
	v_mov_b32_e32 v57, v53
	v_mov_b32_e32 v26, v38
	v_mov_b32_e32 v71, v69
	v_mov_b32_e32 v56, v40
	v_mov_b32_e32 v70, v24
	v_mov_b32_e32 v27, v23
	v_mov_b32_e32 v39, v47
	v_pk_mul_f32 v[22:23], v[46:47], v[22:23]
	v_mov_b32_e32 v41, v17
	v_pk_mul_f32 v[16:17], v[16:17], v[52:53]
	v_mov_b32_e32 v25, v19
	v_pk_mul_f32 v[18:19], v[18:19], v[68:69]
	v_pk_mul_f32 v[46:47], v[64:65], v[72:73]
	v_pk_mul_f32 v[44:45], v[50:51], v[44:45]
	v_pk_mul_f32 v[52:53], v[58:59], v[54:55]
	v_pk_fma_f32 v[26:27], v[38:39], v[26:27], v[46:47]
	v_pk_mul_f32 v[22:23], v[46:47], v[22:23]
	v_pk_fma_f32 v[54:55], v[40:41], v[56:57], v[44:45]
	v_pk_mul_f32 v[16:17], v[44:45], v[16:17]
	v_pk_fma_f32 v[56:57], v[24:25], v[70:71], v[52:53]
	v_pk_mul_f32 v[18:19], v[52:53], v[18:19]
	v_mov_b32_e32 v27, v23
	v_mov_b32_e32 v55, v17
	v_mov_b32_e32 v57, v19
	v_pk_add_f32 v[16:17], v[60:61], v[54:55]
	v_pk_add_f32 v[18:19], v[26:27], v[56:57]
	s_nop 0
	v_pk_add_f32 v[16:17], v[16:17], v[18:19]
	s_nop 0
	v_add_f32_e32 v16, v16, v17
	ds_bpermute_b32 v17, v30, v16
	s_waitcnt lgkmcnt(0)
	v_add_f32_e32 v16, v16, v17
	ds_bpermute_b32 v17, v31, v16
	s_waitcnt lgkmcnt(0)
	v_add_f32_e32 v16, v16, v17
	ds_bpermute_b32 v17, v32, v16
	s_waitcnt lgkmcnt(0)
	v_add_f32_e32 v16, v16, v17
	ds_bpermute_b32 v17, v33, v16
	s_waitcnt lgkmcnt(0)
	v_add_f32_e32 v16, v16, v17
	ds_bpermute_b32 v17, v34, v16
	s_waitcnt lgkmcnt(0)
	v_add_f32_e32 v16, v16, v17
	ds_bpermute_b32 v17, v35, v16
	s_waitcnt lgkmcnt(0)
	v_add_f32_e32 v16, v16, v17
	v_fmamk_f32 v16, v16, 0x3aaaaaab, v36
	v_mul_f32_e32 v17, 0x4b800000, v16
	v_cmp_gt_f32_e32 vcc, s22, v16
	s_nop 1
	v_cndmask_b32_e32 v16, v16, v17, vcc
	v_rsq_f32_e32 v16, v16
	s_nop 0
	v_mul_f32_e32 v17, 0x45800000, v16
	v_cndmask_b32_e32 v16, v16, v17, vcc
	v_mul_f32_e32 v17, v48, v16
	v_mul_f32_e32 v18, v20, v16
	v_mul_f32_e32 v19, v40, v16
	v_mul_f32_e32 v20, v50, v16
	v_mul_f32_e32 v2, v2, v17
	v_mul_f32_e32 v3, v3, v18
	v_mul_f32_e32 v4, v4, v19
	v_mul_f32_e32 v5, v5, v20
	v_cvt_pk_bf16_f32 v2, v2, v3
	v_cvt_pk_bf16_f32 v3, v4, v5
	global_store_dwordx2 v[28:29], v[2:3], off
	v_mov_b32_e32 v2, v142
	v_mov_b32_e32 v3, v143
	v_mov_b32_e32 v4, v144
	v_mov_b32_e32 v5, v145
	v_mul_f32_e32 v17, v64, v16
	v_mul_f32_e32 v18, v38, v16
	v_mul_f32_e32 v19, v24, v16
	v_mul_f32_e32 v20, v58, v16
	v_mul_f32_e32 v2, v2, v17
	v_mul_f32_e32 v3, v3, v18
	v_mul_f32_e32 v4, v4, v19
	v_mul_f32_e32 v5, v5, v20
	v_cvt_pk_bf16_f32 v2, v2, v3
	v_cvt_pk_bf16_f32 v3, v4, v5
	global_store_dwordx2 v[28:29], v[2:3], off offset:512
	v_mov_b32_e32 v2, v146
	v_mov_b32_e32 v3, v147
	v_mov_b32_e32 v4, v148
	v_mov_b32_e32 v5, v149
	v_mul_f32_e32 v17, v43, v16
	v_mul_f32_e32 v18, v45, v16
	v_mul_f32_e32 v19, v53, v16
	v_mul_f32_e32 v16, v47, v16
	v_mul_f32_e32 v2, v2, v17
	v_mul_f32_e32 v3, v3, v18
	v_mul_f32_e32 v4, v4, v19
	v_mul_f32_e32 v5, v5, v16
	v_cvt_pk_bf16_f32 v2, v2, v3
	v_cvt_pk_bf16_f32 v3, v4, v5
	global_store_dwordx2 v[28:29], v[2:3], off offset:1024
	s_cbranch_scc1 .LBB0_1174

.LBB0_2281:
	global_load_dwordx4 v[142:145], v[8:9], off
	global_load_dwordx4 v[146:149], v[10:11], off
	v_lshl_add_u64 v[20:21], s[86:87], 0, v[18:19]
	v_add_co_u32_e32 v38, vcc, 0x53c00000, v20
	v_lshl_add_u64 v[24:25], s[86:87], 0, v[16:17]
	s_nop 0
	v_addc_co_u32_e32 v39, vcc, 0, v21, vcc
	v_add_co_u32_e32 v20, vcc, 0x57200000, v20
	v_lshl_add_u64 v[26:27], s[86:87], 0, v[14:15]
	s_nop 0
	v_addc_co_u32_e32 v21, vcc, 0, v21, vcc
	v_add_co_u32_e32 v24, vcc, 0x9d00000, v24
	global_load_dwordx4 v[2:5], v[6:7], off offset:3072
	global_load_dwordx2 v[40:41], v[38:39], off
	global_load_dwordx2 v[42:43], v[38:39], off offset:512
	v_addc_co_u32_e32 v25, vcc, 0, v25, vcc
	global_load_dwordx2 v[44:45], v[20:21], off
	global_load_dwordx2 v[46:47], v[20:21], off offset:512
	global_load_dwordx2 v[48:49], v[38:39], off offset:1024
	v_add_co_u32_e32 v26, vcc, 0x34400000, v26
	global_load_dwordx2 v[38:39], v[24:25], off
	global_load_dwordx2 v[50:51], v[24:25], off offset:512
	global_load_dwordx2 v[52:53], v[20:21], off offset:1024
	v_addc_co_u32_e32 v27, vcc, 0, v27, vcc
	global_load_dwordx2 v[20:21], v[26:27], off
	global_load_dwordx2 v[54:55], v[26:27], off offset:512
	global_load_dwordx2 v[56:57], v[26:27], off offset:1024
	global_load_dwordx2 v[58:59], v[24:25], off offset:1024
	v_mov_b32_e32 v80, 0
	v_lshl_add_u64 v[22:23], s[86:87], 0, v[12:13]
	v_add_co_u32_e64 v22, s[6:7], s16, v22
	s_add_i32 s2, s2, s4
	s_nop 0
	v_addc_co_u32_e64 v23, s[6:7], 0, v23, s[6:7]
	v_lshl_add_u64 v[12:13], v[12:13], 0, s[8:9]
	v_lshl_add_u64 v[14:15], v[14:15], 0, s[10:11]
	v_lshl_add_u64 v[16:17], v[16:17], 0, s[12:13]
	v_lshl_add_u64 v[18:19], v[18:19], 0, s[14:15]
	s_cmp_lt_i32 s2, 0x8000
	s_waitcnt vmcnt(11)
	v_lshlrev_b32_e32 v25, 16, v40
	v_and_b32_e32 v27, 0xffff0000, v40
	s_waitcnt vmcnt(10)
	v_lshlrev_b32_e32 v61, 16, v42
	v_and_b32_e32 v62, 0xffff0000, v42
	s_waitcnt vmcnt(9)
	v_lshlrev_b32_e32 v40, 16, v44
	v_and_b32_e32 v42, 0xffff0000, v44
	v_lshlrev_b32_e32 v60, 16, v41
	v_and_b32_e32 v41, 0xffff0000, v41
	v_lshlrev_b32_e32 v63, 16, v43
	v_and_b32_e32 v43, 0xffff0000, v43
	v_lshlrev_b32_e32 v44, 16, v45
	v_and_b32_e32 v45, 0xffff0000, v45
	s_waitcnt vmcnt(8)
	v_lshlrev_b32_e32 v64, 16, v46
	v_and_b32_e32 v65, 0xffff0000, v46
	v_lshlrev_b32_e32 v66, 16, v47
	v_and_b32_e32 v47, 0xffff0000, v47
	s_waitcnt vmcnt(7)
	v_and_b32_e32 v24, 0xffff0000, v48
	v_and_b32_e32 v26, 0xffff0000, v49
	v_add_f32_e32 v40, v40, v25
	v_add_f32_e32 v42, v42, v27
	s_waitcnt vmcnt(4)
	v_and_b32_e32 v25, 0xffff0000, v52
	v_and_b32_e32 v27, 0xffff0000, v53
	v_lshlrev_b32_e32 v67, 16, v48
	v_lshlrev_b32_e32 v68, 16, v49
	v_lshlrev_b32_e32 v49, 16, v38
	v_and_b32_e32 v69, 0xffff0000, v38
	v_add_f32_e32 v38, v44, v60
	v_lshlrev_b32_e32 v70, 16, v39
	v_add_f32_e32 v44, v45, v41
	v_and_b32_e32 v39, 0xffff0000, v39
	v_add_f32_e32 v46, v64, v61
	v_lshlrev_b32_e32 v41, 16, v50
	v_add_f32_e32 v48, v65, v62
	v_and_b32_e32 v45, 0xffff0000, v50
	v_add_f32_e32 v50, v66, v63
	v_lshlrev_b32_e32 v61, 16, v51
	v_add_f32_e32 v60, v47, v43
	v_and_b32_e32 v43, 0xffff0000, v51
	v_lshlrev_b32_e32 v47, 16, v52
	v_lshlrev_b32_e32 v51, 16, v53
	s_waitcnt vmcnt(3)
	v_lshlrev_b32_e32 v52, 16, v20
	v_and_b32_e32 v65, 0xffff0000, v21
	s_waitcnt vmcnt(2)
	v_lshlrev_b32_e32 v66, 16, v54
	v_and_b32_e32 v71, 0xffff0000, v55
	v_pk_add_f32 v[24:25], v[24:25], v[24:25] op_sel_hi:[0,1]
	v_pk_add_f32 v[26:27], v[26:27], v[26:27] op_sel_hi:[0,1]
	v_fmac_f32_e32 v42, v1, v69
	v_fmac_f32_e32 v38, v1, v70
	v_fmac_f32_e32 v44, v1, v39
	v_and_b32_e32 v62, 0xffff0000, v20
	v_lshlrev_b32_e32 v64, 16, v21
	v_fmac_f32_e32 v60, v28, v43
	v_and_b32_e32 v69, 0xffff0000, v54
	v_lshlrev_b32_e32 v70, 16, v55
	s_waitcnt vmcnt(0)
	v_lshlrev_b32_e32 v20, 16, v58
	v_and_b32_e32 v24, 0xffff0000, v58
	v_add_f32_e32 v53, v68, v51
	v_lshlrev_b32_e32 v39, 16, v59
	v_and_b32_e32 v26, 0xffff0000, v59
	v_lshlrev_b32_e32 v55, 16, v56
	v_and_b32_e32 v59, 0xffff0000, v56
	v_lshlrev_b32_e32 v63, 16, v57
	v_and_b32_e32 v57, 0xffff0000, v57
	v_mul_f32_e32 v43, 0xbfb8aa3b, v52
	v_mul_f32_e32 v54, 0xbfb8aa3b, v65
	v_mul_f32_e32 v56, 0xbfb8aa3b, v66
	v_mul_f32_e32 v68, 0xbfb8aa3b, v71
	v_fmac_f32_e32 v40, v1, v49
	v_fmac_f32_e32 v46, v28, v41
	v_fmac_f32_e32 v48, v28, v45
	v_fmac_f32_e32 v50, v28, v61
	v_add_f32_e32 v21, v67, v47
	v_mul_f32_e32 v49, 0xbfb8aa3b, v62
	v_mul_f32_e32 v51, 0xbfb8aa3b, v64
	v_mul_f32_e32 v58, 0xbfb8aa3b, v69
	v_mul_f32_e32 v67, 0xbfb8aa3b, v70
	v_mul_f32_e32 v41, v29, v20
	v_mul_f32_e32 v45, v29, v24
	v_mul_f32_e32 v61, v29, v39
	v_mul_f32_e32 v47, v29, v26
	v_mul_f32_e32 v20, 0xbfb8aa3b, v55
	v_mul_f32_e32 v24, 0xbfb8aa3b, v59
	v_mul_f32_e32 v26, 0xbfb8aa3b, v63
	v_mul_f32_e32 v39, 0xbfb8aa3b, v57
	v_exp_f32_e32 v43, v43
	v_exp_f32_e32 v54, v54
	v_exp_f32_e32 v56, v56
	v_exp_f32_e32 v68, v68
	v_exp_f32_e32 v49, v49
	v_exp_f32_e32 v51, v51
	v_exp_f32_e32 v58, v58
	v_exp_f32_e32 v67, v67
	v_exp_f32_e32 v20, v20
	v_exp_f32_e32 v24, v24
	v_exp_f32_e32 v26, v26
	v_exp_f32_e32 v39, v39
	v_add_f32_e32 v43, 1.0, v43
	v_add_f32_e32 v54, 1.0, v54
	v_add_f32_e32 v56, 1.0, v56
	v_add_f32_e32 v68, 1.0, v68
	v_add_f32_e32 v49, 1.0, v49
	v_add_f32_e32 v51, 1.0, v51
	v_add_f32_e32 v58, 1.0, v58
	v_add_f32_e32 v67, 1.0, v67
	v_add_f32_e32 v20, 1.0, v20
	v_add_f32_e32 v24, 1.0, v24
	v_add_f32_e32 v26, 1.0, v26
	v_add_f32_e32 v72, 1.0, v39
	v_rcp_f32_e32 v73, v43
	v_rcp_f32_e32 v76, v54
	v_rcp_f32_e32 v56, v56
	v_rcp_f32_e32 v68, v68
	v_rcp_f32_e32 v74, v49
	v_rcp_f32_e32 v75, v51
	v_rcp_f32_e32 v77, v58
	v_rcp_f32_e32 v67, v67
	v_rcp_f32_e32 v43, v20
	v_rcp_f32_e32 v39, v24
	v_rcp_f32_e32 v51, v26
	v_rcp_f32_e32 v49, v72
	v_mul_f32_e32 v20, v73, v52
	v_mul_f32_e32 v24, v76, v65
	v_mul_f32_e32 v26, v56, v66
	v_mul_f32_e32 v52, v68, v71
	v_mul_f32_e32 v54, v74, v62
	v_mul_f32_e32 v58, v75, v64
	v_mul_f32_e32 v56, v77, v69
	v_mul_f32_e32 v62, v67, v70
	v_pk_mul_f32 v[64:65], v[20:21], v[40:41]
	v_pk_add_f32 v[66:67], v[20:21], v[40:41]
	v_pk_mul_f32 v[68:69], v[24:25], v[44:45]
	v_pk_add_f32 v[70:71], v[24:25], v[44:45]
	v_pk_mul_f32 v[72:73], v[52:53], v[60:61]
	v_pk_add_f32 v[74:75], v[52:53], v[60:61]
	v_pk_mul_f32 v[76:77], v[26:27], v[46:47]
	v_pk_add_f32 v[78:79], v[26:27], v[46:47]
	v_mov_b32_e32 v41, v43
	v_mov_b32_e32 v21, v55
	v_mov_b32_e32 v45, v39
	v_mov_b32_e32 v25, v59
	v_mov_b32_e32 v61, v51
	v_mov_b32_e32 v53, v63
	v_mov_b32_e32 v47, v49
	v_mov_b32_e32 v27, v57
	v_pk_mul_f32 v[42:43], v[42:43], v[54:55]
	v_pk_mul_f32 v[38:39], v[38:39], v[58:59]
	v_pk_mul_f32 v[50:51], v[50:51], v[62:63]
	v_pk_mul_f32 v[48:49], v[48:49], v[56:57]
	v_mov_b32_e32 v65, v67
	v_mov_b32_e32 v69, v71
	v_mov_b32_e32 v73, v75
	v_mov_b32_e32 v77, v79
	v_pk_mul_f32 v[20:21], v[40:41], v[20:21]
	v_pk_mul_f32 v[24:25], v[44:45], v[24:25]
	v_pk_mul_f32 v[52:53], v[60:61], v[52:53]
	v_pk_mul_f32 v[26:27], v[46:47], v[26:27]
	v_mov_b32_e32 v40, v42
	v_mov_b32_e32 v41, v67
	v_pk_mul_f32 v[54:55], v[66:67], v[42:43]
	v_mov_b32_e32 v44, v38
	v_mov_b32_e32 v45, v71
	v_pk_mul_f32 v[56:57], v[70:71], v[38:39]
	v_mov_b32_e32 v58, v50
	v_mov_b32_e32 v59, v75
	v_pk_mul_f32 v[60:61], v[74:75], v[50:51]
	v_mov_b32_e32 v46, v48
	v_mov_b32_e32 v47, v79
	v_pk_mul_f32 v[62:63], v[78:79], v[48:49]
	v_pk_mul_f32 v[20:21], v[64:65], v[20:21]
	v_pk_mul_f32 v[24:25], v[68:69], v[24:25]
	v_pk_mul_f32 v[52:53], v[72:73], v[52:53]
	v_pk_mul_f32 v[26:27], v[76:77], v[26:27]
	v_pk_fma_f32 v[40:41], v[40:41], v[42:43], v[20:21]
	v_pk_mul_f32 v[54:55], v[20:21], v[54:55]
	v_pk_fma_f32 v[44:45], v[44:45], v[38:39], v[24:25]
	v_pk_mul_f32 v[56:57], v[24:25], v[56:57]
	v_pk_fma_f32 v[58:59], v[58:59], v[50:51], v[52:53]
	v_pk_mul_f32 v[60:61], v[52:53], v[60:61]
	v_pk_fma_f32 v[46:47], v[46:47], v[48:49], v[26:27]
	v_pk_mul_f32 v[62:63], v[26:27], v[62:63]
	v_mov_b32_e32 v41, v55
	v_mov_b32_e32 v45, v57
	v_mov_b32_e32 v59, v61
	v_mov_b32_e32 v47, v63
	v_pk_add_f32 v[40:41], v[40:41], v[44:45]
	v_pk_add_f32 v[44:45], v[46:47], v[58:59]
	s_nop 0
	v_pk_add_f32 v[40:41], v[40:41], v[44:45]
	s_nop 0
	v_add_f32_e32 v20, v40, v41
	ds_bpermute_b32 v24, v30, v20
	s_waitcnt lgkmcnt(0)
	v_add_f32_e32 v20, v20, v24
	ds_bpermute_b32 v24, v31, v20
	s_waitcnt lgkmcnt(0)
	v_add_f32_e32 v20, v20, v24
	ds_bpermute_b32 v24, v32, v20
	s_waitcnt lgkmcnt(0)
	v_add_f32_e32 v20, v20, v24
	ds_bpermute_b32 v24, v33, v20
	s_waitcnt lgkmcnt(0)
	v_add_f32_e32 v20, v20, v24
	ds_bpermute_b32 v24, v34, v20
	s_waitcnt lgkmcnt(0)
	v_add_f32_e32 v20, v20, v24
	ds_bpermute_b32 v24, v35, v20
	s_waitcnt lgkmcnt(0)
	v_add_f32_e32 v20, v20, v24
	v_fmamk_f32 v20, v20, 0x3aaaaaab, v36
	v_mul_f32_e32 v24, 0x4b800000, v20
	v_cmp_gt_f32_e32 vcc, s3, v20
	s_nop 1
	v_cndmask_b32_e32 v20, v20, v24, vcc
	v_rsq_f32_e32 v20, v20
	s_nop 0
	v_mul_f32_e32 v24, 0x45800000, v20
	v_cndmask_b32_e32 v20, v20, v24, vcc
	v_mul_f32_e32 v24, v64, v20
	v_mul_f32_e32 v26, v42, v20
	v_mul_f32_e32 v2, v2, v24
	v_mul_f32_e32 v3, v3, v26
	v_med3_f32 v2, v2, s5, v37
	v_med3_f32 v3, v3, s5, v37
	v_cvt_pk_fp8_f32 v80, v2, v3
	v_mul_f32_e32 v38, v38, v20
	v_mul_f32_e32 v39, v68, v20
	v_mul_f32_e32 v4, v4, v38
	v_mul_f32_e32 v5, v5, v39
	v_med3_f32 v4, v4, s5, v37
	v_med3_f32 v5, v5, s5, v37
	v_cvt_pk_fp8_f32 v80, v4, v5 op_sel:[0,0,1]
	v_mul_f32_e32 v26, v76, v20
	v_mul_f32_e32 v38, v48, v20
	v_mov_b32_e32 v24, 0
	global_store_dword v[22:23], v80, off
	v_mov_b32_e32 v2, v142
	v_mov_b32_e32 v3, v143
	v_mov_b32_e32 v4, v144
	v_mov_b32_e32 v5, v145
	v_mul_f32_e32 v39, v50, v20
	v_mul_f32_e32 v40, v72, v20
	v_mul_f32_e32 v21, v21, v20
	v_mul_f32_e32 v25, v25, v20
	v_mul_f32_e32 v2, v2, v26
	v_mul_f32_e32 v3, v3, v38
	v_med3_f32 v2, v2, s5, v37
	v_med3_f32 v3, v3, s5, v37
	v_cvt_pk_fp8_f32 v24, v2, v3
	v_mul_f32_e32 v4, v4, v39
	v_mul_f32_e32 v5, v5, v40
	v_med3_f32 v4, v4, s5, v37
	v_med3_f32 v5, v5, s5, v37
	v_cvt_pk_fp8_f32 v24, v4, v5 op_sel:[0,0,1]
	v_mul_f32_e32 v26, v53, v20
	v_mul_f32_e32 v20, v27, v20
	global_store_dword v[22:23], v24, off offset:256
	v_mov_b32_e32 v2, v146
	v_mov_b32_e32 v3, v147
	v_mov_b32_e32 v4, v148
	v_mov_b32_e32 v5, v149
	v_mov_b32_e32 v24, 0
	v_mul_f32_e32 v2, v2, v21
	v_mul_f32_e32 v3, v3, v25
	v_med3_f32 v2, v2, s5, v37
	v_med3_f32 v3, v3, s5, v37
	v_cvt_pk_fp8_f32 v24, v2, v3
	v_mul_f32_e32 v4, v4, v26
	v_mul_f32_e32 v2, v5, v20
	v_med3_f32 v3, v4, s5, v37
	v_med3_f32 v2, v2, s5, v37
	v_cvt_pk_fp8_f32 v24, v3, v2 op_sel:[0,0,1]
	global_store_dword v[22:23], v24, off offset:512
	s_cbranch_scc1 .LBB0_2281
